# grid barrier: blocks that are not their XCD's last arriver invalidate only L1 (buffer_inv sc0); the XCD's last arriver still invalidates L2 before it releases the others
# speedup vs baseline: 1.0164x; 1.0164x over previous
.LBB0_126:
	s_or_b64 exec, exec, s[6:7]
	s_waitcnt vmcnt(0) lgkmcnt(0)
	buffer_inv sc0
	s_waitcnt vmcnt(0)

.LBB0_257:
	s_or_b64 exec, exec, s[4:5]
	s_waitcnt vmcnt(0) lgkmcnt(0)
	buffer_inv sc0
	s_waitcnt vmcnt(0)
